# vt8fuse: V^T fp8 tiles written directly by the layer-1 QKV GEMM epilogue (per-wave LDS byte placement, 1 KB-contiguous stores); the transposition phase and its grid barrier dropped
# speedup vs baseline: 1.0050x; 1.0040x over previous
.LBB0_973:
	s_and_b32 s98, s46, 3
	s_lshl_b32 s98, s98, 1
	s_mov_b32 s99, s47
	v_and_b32_e32 v250, 63, v0
	v_and_b32_e32 v251, 15, v250
	v_lshrrev_b32_e32 v249, 4, v250
	v_readfirstlane_b32 s100, v0
	s_lshr_b32 s100, s100, 6
	s_lshl_b32 s101, s100, 11
	s_add_i32 s101, s101, 0xc000
	v_lshl_add_u32 v245, v250, 4, s101
	v_lshrrev_b32_e32 v248, 2, v251
	v_xor_b32_e32 v248, v248, v249
	v_and_b32_e32 v248, 1, v248
	v_lshlrev_b32_e32 v248, 5, v248
	v_lshl_add_u32 v248, v249, 9, v248
	v_and_b32_e32 v247, 3, v251
	v_add_u32_e32 v248, v248, v247
	v_lshrrev_b32_e32 v247, 3, v251
	v_lshl_add_u32 v248, v247, 2, v248
	v_add_u32_e32 v244, s101, v248
	s_and_b32 s101, s100, 3
	s_lshl_b32 s101, s101, 11
	v_lshl_add_u32 v252, v250, 4, s101
	s_ashr_i32 s6, s46, 2
	s_cmp_gt_i32 s6, 1
	s_cselect_b64 s[42:43], -1, 0
	s_cmp_lt_i32 s6, 2
	v_lshl_add_u32 v6, s47, 8, v200
	s_cselect_b64 s[4:5], -1, 0
	s_cmpk_lt_i32 s47, 0x80
	v_lshrrev_b32_e32 v2, 1, v201
	s_cselect_b64 s[44:45], -1, 0
	v_and_b32_e32 v30, 28, v2
	v_lshlrev_b32_e32 v2, 5, v6
	v_and_or_b32 v2, v2, s64, v30
	s_and_b64 s[44:45], s[4:5], s[44:45]
	v_lshlrev_b32_e32 v194, 3, v2
	v_cndmask_b32_e64 v2, 0, 1, s[44:45]
	v_pk_mul_f32 v[24:25], v[192:193], s[28:29] op_sel_hi:[1,0]
	v_pk_mul_f32 v[18:19], v[190:191], s[28:29] op_sel_hi:[1,0]
	v_pk_mul_f32 v[22:23], v[188:189], s[28:29] op_sel_hi:[1,0]
	v_pk_mul_f32 v[20:21], v[186:187], s[28:29] op_sel_hi:[1,0]
	v_cmp_ne_u32_e64 s[4:5], 1, v2
	s_andn2_b64 vcc, exec, s[44:45]
	v_lshl_add_u64 v[14:15], s[18:19], 0, v[194:195]
	s_cbranch_vccnz .LBB0_975
	global_load_dwordx4 v[2:5], v[14:15], off
	global_load_dwordx4 v[8:11], v[14:15], off offset:16
	s_waitcnt vmcnt(1)
	v_pk_mul_f32 v[16:17], v[18:19], v[2:3] op_sel:[1,1] op_sel_hi:[1,0]
	v_mul_f32_e32 v32, v25, v5
	v_mul_f32_e32 v34, v25, v4
	s_waitcnt vmcnt(0)
	v_pk_mul_f32 v[38:39], v[20:21], v[8:9] op_sel:[1,1] op_sel_hi:[1,0]
	v_mul_f32_e32 v40, v23, v11
	v_mul_f32_e32 v42, v23, v10
	v_pk_mul_f32 v[12:13], v[18:19], v[2:3]
	v_pk_mul_f32 v[36:37], v[20:21], v[8:9]
	v_pk_fma_f32 v[18:19], v[18:19], v[2:3], v[16:17] op_sel_hi:[0,1,1]
	v_pk_fma_f32 v[2:3], v[24:25], v[4:5], v[32:33] op_sel_hi:[1,1,0] neg_lo:[0,0,1] neg_hi:[0,0,1]
	v_pk_fma_f32 v[4:5], v[24:25], v[4:5], v[34:35] op_sel:[0,1,0] op_sel_hi:[1,0,0]
	v_pk_fma_f32 v[20:21], v[20:21], v[8:9], v[38:39] op_sel_hi:[0,1,1]
	v_pk_fma_f32 v[8:9], v[22:23], v[10:11], v[40:41] op_sel_hi:[1,1,0] neg_lo:[0,0,1] neg_hi:[0,0,1]
	v_pk_fma_f32 v[10:11], v[22:23], v[10:11], v[42:43] op_sel:[0,1,0] op_sel_hi:[1,0,0]
	v_sub_f32_e32 v20, v36, v38
	v_sub_f32_e32 v18, v12, v16
	v_mov_b32_e32 v22, v8
	v_mov_b32_e32 v23, v10
	v_mov_b32_e32 v24, v2
	v_mov_b32_e32 v25, v4
.LBB0_975:
	s_lshl_b32 s7, s46, 8
	s_and_b32 s7, s7, 0x300
	v_or_b32_e32 v10, s7, v201
	s_mul_hi_i32 s7, s6, 0x4100000
	s_mul_i32 s6, s6, 0x4100000
	s_add_u32 s44, s55, s6
	s_addc_u32 s45, s56, s7
	s_cmp_lt_u32 s46, 4
	s_cselect_b64 s[6:7], -1, 0
	v_lshlrev_b32_e32 v194, 1, v10
	v_ashrrev_i32_e32 v7, 31, v6
	v_cndmask_b32_e64 v2, 1.0, v214, s[6:7]
	v_lshl_add_u64 v[8:9], s[44:45], 0, v[194:195]
	v_lshlrev_b64 v[4:5], 11, v[6:7]
	v_mov_b32_e32 v3, v2
	v_lshl_add_u64 v[12:13], v[8:9], 0, v[4:5]
	s_mov_b64 s[46:47], -1
	s_and_b64 vcc, exec, s[42:43]
	s_cbranch_vccz .LBB0_977
	v_mov_b32_e32 v4, v2
	v_mov_b32_e32 v5, v2
	v_pk_mul_f32 v[32:33], v[2:3], v[18:19]
	v_pk_mul_f32 v[34:35], v[2:3], v[20:21]
	v_pk_mul_f32 v[16:17], v[4:5], v[24:25]
	v_pk_mul_f32 v[4:5], v[4:5], v[22:23]
	v_cvt_pk_bf16_f32 v32, v32, v33
	v_cvt_pk_bf16_f32 v33, v16, v17
	v_cvt_pk_bf16_f32 v34, v34, v35
	s_mov_b64 s[46:47], 0
	v_cvt_pk_bf16_f32 v35, v4, v5
	v_lshlrev_b32_e32 v224, 16, v32
	v_and_b32_e32 v225, 0xffff0000, v32
	v_lshlrev_b32_e32 v226, 16, v33
	v_and_b32_e32 v227, 0xffff0000, v33
	v_lshlrev_b32_e32 v228, 16, v34
	v_and_b32_e32 v229, 0xffff0000, v34
	v_lshlrev_b32_e32 v230, 16, v35
	v_and_b32_e32 v231, 0xffff0000, v35
	v_cvt_pk_fp8_f32 v232, v224, v225
	v_cvt_pk_fp8_f32 v233, v228, v229
	v_cvt_pk_fp8_f32 v232, v226, v227 op_sel:[0,0,1]
	v_cvt_pk_fp8_f32 v233, v230, v231 op_sel:[0,0,1]
	v_lshrrev_b32_e32 v234, 8, v232
	v_lshrrev_b32_e32 v235, 8, v233
	ds_write_b8 v244, v232 offset:0
	ds_write_b8 v244, v234 offset:64
	ds_write_b8_d16_hi v244, v232 offset:128
	ds_write_b8_d16_hi v244, v234 offset:192
	ds_write_b8 v244, v233 offset:272
	ds_write_b8 v244, v235 offset:336
	ds_write_b8_d16_hi v244, v233 offset:400
	ds_write_b8_d16_hi v244, v235 offset:464

.LBB0_981:
	v_cndmask_b32_e64 v7, 0, 1, s[42:43]
	v_cmp_ne_u32_e64 s[6:7], 1, v7
	s_andn2_b64 vcc, exec, s[42:43]
	s_mov_b64 s[42:43], -1
	s_cbranch_vccnz .LBB0_983
	v_mov_b32_e32 v14, v2
	v_mov_b32_e32 v15, v2
	v_pk_mul_f32 v[34:35], v[14:15], v[22:23]
	v_pk_mul_f32 v[32:33], v[2:3], v[18:19]
	s_mov_b64 s[42:43], 0
	v_pk_mul_f32 v[14:15], v[14:15], v[20:21]
	v_pk_mul_f32 v[36:37], v[2:3], v[24:25]
	v_cvt_pk_bf16_f32 v32, v32, v33
	v_cvt_pk_bf16_f32 v33, v34, v35
	s_nop 0
	v_cvt_pk_bf16_f32 v34, v36, v37
	v_cvt_pk_bf16_f32 v35, v14, v15
	v_lshlrev_b32_e32 v224, 16, v32
	v_and_b32_e32 v225, 0xffff0000, v32
	v_lshlrev_b32_e32 v226, 16, v33
	v_and_b32_e32 v227, 0xffff0000, v33
	v_lshlrev_b32_e32 v228, 16, v34
	v_and_b32_e32 v229, 0xffff0000, v34
	v_lshlrev_b32_e32 v230, 16, v35
	v_and_b32_e32 v231, 0xffff0000, v35
	v_cvt_pk_fp8_f32 v232, v224, v225
	v_cvt_pk_fp8_f32 v233, v228, v229
	v_cvt_pk_fp8_f32 v232, v226, v227 op_sel:[0,0,1]
	v_cvt_pk_fp8_f32 v233, v230, v231 op_sel:[0,0,1]
	v_mov_b32_e32 v236, v232
	v_mov_b32_e32 v237, v233

.LBB0_987:
	v_ashrrev_i32_e32 v15, 31, v14
	v_lshlrev_b64 v[12:13], 11, v[14:15]
	v_lshl_add_u64 v[12:13], v[8:9], 0, v[12:13]
	s_and_b64 vcc, exec, s[6:7]
	s_mov_b64 s[42:43], -1
	s_cbranch_vccnz .LBB0_989
	v_mov_b32_e32 v32, v2
	v_mov_b32_e32 v33, v2
	v_pk_mul_f32 v[34:35], v[32:33], v[24:25]
	s_mov_b64 s[42:43], 0
	v_pk_mul_f32 v[36:37], v[2:3], v[18:19]
	v_pk_mul_f32 v[38:39], v[32:33], v[22:23]
	v_pk_mul_f32 v[40:41], v[2:3], v[20:21]
	v_cvt_pk_bf16_f32 v32, v36, v37
	v_cvt_pk_bf16_f32 v33, v34, v35
	s_nop 0
	v_cvt_pk_bf16_f32 v34, v40, v41
	v_cvt_pk_bf16_f32 v35, v38, v39
	v_lshlrev_b32_e32 v224, 16, v32
	v_and_b32_e32 v225, 0xffff0000, v32
	v_lshlrev_b32_e32 v226, 16, v33
	v_and_b32_e32 v227, 0xffff0000, v33
	v_lshlrev_b32_e32 v228, 16, v34
	v_and_b32_e32 v229, 0xffff0000, v34
	v_lshlrev_b32_e32 v230, 16, v35
	v_and_b32_e32 v231, 0xffff0000, v35
	v_cvt_pk_fp8_f32 v232, v224, v225
	v_cvt_pk_fp8_f32 v233, v228, v229
	v_cvt_pk_fp8_f32 v232, v226, v227 op_sel:[0,0,1]
	v_cvt_pk_fp8_f32 v233, v230, v231 op_sel:[0,0,1]
	v_lshrrev_b32_e32 v234, 8, v232
	v_lshrrev_b32_e32 v235, 8, v233
	ds_write_b8 v244, v232 offset:8
	ds_write_b8 v244, v234 offset:72
	ds_write_b8_d16_hi v244, v232 offset:136
	ds_write_b8_d16_hi v244, v234 offset:200
	ds_write_b8 v244, v233 offset:280
	ds_write_b8 v244, v235 offset:344
	ds_write_b8_d16_hi v244, v233 offset:408
	ds_write_b8_d16_hi v244, v235 offset:472

.LBB0_997:
	v_ashrrev_i32_e32 v15, 31, v14
	v_lshlrev_b64 v[12:13], 11, v[14:15]
	v_lshl_add_u64 v[12:13], v[8:9], 0, v[12:13]
	s_and_b64 vcc, exec, s[6:7]
	s_mov_b64 s[42:43], -1
	s_cbranch_vccnz .LBB0_999
	v_mov_b32_e32 v32, v2
	v_mov_b32_e32 v33, v2
	v_pk_mul_f32 v[34:35], v[32:33], v[24:25]
	s_mov_b64 s[42:43], 0
	v_pk_mul_f32 v[36:37], v[2:3], v[18:19]
	v_pk_mul_f32 v[38:39], v[32:33], v[22:23]
	v_pk_mul_f32 v[40:41], v[2:3], v[20:21]
	v_cvt_pk_bf16_f32 v32, v36, v37
	v_cvt_pk_bf16_f32 v33, v34, v35
	s_nop 0
	v_cvt_pk_bf16_f32 v34, v40, v41
	v_cvt_pk_bf16_f32 v35, v38, v39
	v_lshlrev_b32_e32 v224, 16, v32
	v_and_b32_e32 v225, 0xffff0000, v32
	v_lshlrev_b32_e32 v226, 16, v33
	v_and_b32_e32 v227, 0xffff0000, v33
	v_lshlrev_b32_e32 v228, 16, v34
	v_and_b32_e32 v229, 0xffff0000, v34
	v_lshlrev_b32_e32 v230, 16, v35
	v_and_b32_e32 v231, 0xffff0000, v35
	v_cvt_pk_fp8_f32 v232, v224, v225
	v_cvt_pk_fp8_f32 v233, v228, v229
	v_cvt_pk_fp8_f32 v232, v226, v227 op_sel:[0,0,1]
	v_cvt_pk_fp8_f32 v233, v230, v231 op_sel:[0,0,1]
	v_lshrrev_b32_e32 v234, 8, v232
	v_lshrrev_b32_e32 v235, 8, v233
	ds_write_b8 v244, v232 offset:16
	ds_write_b8 v244, v234 offset:80
	ds_write_b8_d16_hi v244, v232 offset:144
	ds_write_b8_d16_hi v244, v234 offset:208
	ds_write_b8 v244, v233 offset:256
	ds_write_b8 v244, v235 offset:320
	ds_write_b8_d16_hi v244, v233 offset:384
	ds_write_b8_d16_hi v244, v235 offset:448

.LBB0_1007:
	v_ashrrev_i32_e32 v15, 31, v14
	v_lshlrev_b64 v[12:13], 11, v[14:15]
	v_lshl_add_u64 v[12:13], v[8:9], 0, v[12:13]
	s_and_b64 vcc, exec, s[6:7]
	s_mov_b64 s[42:43], -1
	s_cbranch_vccnz .LBB0_1009
	v_mov_b32_e32 v32, v2
	v_mov_b32_e32 v33, v2
	v_pk_mul_f32 v[34:35], v[32:33], v[24:25]
	s_mov_b64 s[42:43], 0
	v_pk_mul_f32 v[36:37], v[2:3], v[18:19]
	v_pk_mul_f32 v[38:39], v[32:33], v[22:23]
	v_pk_mul_f32 v[40:41], v[2:3], v[20:21]
	v_cvt_pk_bf16_f32 v32, v36, v37
	v_cvt_pk_bf16_f32 v33, v34, v35
	s_nop 0
	v_cvt_pk_bf16_f32 v34, v40, v41
	v_cvt_pk_bf16_f32 v35, v38, v39
	v_lshlrev_b32_e32 v224, 16, v32
	v_and_b32_e32 v225, 0xffff0000, v32
	v_lshlrev_b32_e32 v226, 16, v33
	v_and_b32_e32 v227, 0xffff0000, v33
	v_lshlrev_b32_e32 v228, 16, v34
	v_and_b32_e32 v229, 0xffff0000, v34
	v_lshlrev_b32_e32 v230, 16, v35
	v_and_b32_e32 v231, 0xffff0000, v35
	v_cvt_pk_fp8_f32 v232, v224, v225
	v_cvt_pk_fp8_f32 v233, v228, v229
	v_cvt_pk_fp8_f32 v232, v226, v227 op_sel:[0,0,1]
	v_cvt_pk_fp8_f32 v233, v230, v231 op_sel:[0,0,1]
	v_lshrrev_b32_e32 v234, 8, v232
	v_lshrrev_b32_e32 v235, 8, v233
	ds_write_b8 v244, v232 offset:24
	ds_write_b8 v244, v234 offset:88
	ds_write_b8_d16_hi v244, v232 offset:152
	ds_write_b8_d16_hi v244, v234 offset:216
	ds_write_b8 v244, v233 offset:264
	ds_write_b8 v244, v235 offset:328
	ds_write_b8_d16_hi v244, v233 offset:392
	ds_write_b8_d16_hi v244, v235 offset:456

.LBB0_1017:
	v_ashrrev_i32_e32 v15, 31, v14
	v_lshlrev_b64 v[12:13], 11, v[14:15]
	v_lshl_add_u64 v[12:13], v[8:9], 0, v[12:13]
	s_and_b64 vcc, exec, s[6:7]
	s_mov_b64 s[42:43], -1
	s_cbranch_vccnz .LBB0_1019
	v_mov_b32_e32 v32, v2
	v_mov_b32_e32 v33, v2
	v_pk_mul_f32 v[34:35], v[32:33], v[24:25]
	s_mov_b64 s[42:43], 0
	v_pk_mul_f32 v[36:37], v[2:3], v[18:19]
	v_pk_mul_f32 v[38:39], v[32:33], v[22:23]
	v_pk_mul_f32 v[40:41], v[2:3], v[20:21]
	v_cvt_pk_bf16_f32 v32, v36, v37
	v_cvt_pk_bf16_f32 v33, v34, v35
	s_nop 0
	v_cvt_pk_bf16_f32 v34, v40, v41
	v_cvt_pk_bf16_f32 v35, v38, v39
	v_lshlrev_b32_e32 v224, 16, v32
	v_and_b32_e32 v225, 0xffff0000, v32
	v_lshlrev_b32_e32 v226, 16, v33
	v_and_b32_e32 v227, 0xffff0000, v33
	v_lshlrev_b32_e32 v228, 16, v34
	v_and_b32_e32 v229, 0xffff0000, v34
	v_lshlrev_b32_e32 v230, 16, v35
	v_and_b32_e32 v231, 0xffff0000, v35
	v_cvt_pk_fp8_f32 v232, v224, v225
	v_cvt_pk_fp8_f32 v233, v228, v229
	v_cvt_pk_fp8_f32 v232, v226, v227 op_sel:[0,0,1]
	v_cvt_pk_fp8_f32 v233, v230, v231 op_sel:[0,0,1]
	v_lshrrev_b32_e32 v234, 8, v232
	v_lshrrev_b32_e32 v235, 8, v233
	ds_write_b8 v244, v232 offset:0
	ds_write_b8 v244, v234 offset:64
	ds_write_b8_d16_hi v244, v232 offset:128
	ds_write_b8_d16_hi v244, v234 offset:192
	ds_write_b8 v244, v233 offset:272
	ds_write_b8 v244, v235 offset:336
	ds_write_b8_d16_hi v244, v233 offset:400
	ds_write_b8_d16_hi v244, v235 offset:464

.LBB0_1047:
	v_ashrrev_i32_e32 v19, 31, v18
	v_lshlrev_b64 v[6:7], 11, v[18:19]
	v_lshl_add_u64 v[6:7], v[8:9], 0, v[6:7]
	s_and_b64 vcc, exec, s[6:7]
	s_mov_b64 s[42:43], -1
	s_cbranch_vccnz .LBB0_1049
	v_mov_b32_e32 v8, v2
	v_mov_b32_e32 v9, v2
	v_pk_mul_f32 v[30:31], v[2:3], v[14:15]
	v_pk_mul_f32 v[32:33], v[2:3], v[16:17]
	s_mov_b64 s[42:43], 0
	v_pk_mul_f32 v[24:25], v[8:9], v[22:23]
	v_pk_mul_f32 v[8:9], v[8:9], v[20:21]
	v_cvt_pk_bf16_f32 v30, v30, v31
	v_cvt_pk_bf16_f32 v31, v24, v25
	v_cvt_pk_bf16_f32 v32, v32, v33
	s_nop 0
	v_cvt_pk_bf16_f32 v33, v8, v9
	v_lshlrev_b32_e32 v224, 16, v30
	v_and_b32_e32 v225, 0xffff0000, v30
	v_lshlrev_b32_e32 v226, 16, v31
	v_and_b32_e32 v227, 0xffff0000, v31
	v_lshlrev_b32_e32 v228, 16, v32
	v_and_b32_e32 v229, 0xffff0000, v32
	v_lshlrev_b32_e32 v230, 16, v33
	v_and_b32_e32 v231, 0xffff0000, v33
	v_cvt_pk_fp8_f32 v232, v224, v225
	v_cvt_pk_fp8_f32 v233, v228, v229
	v_cvt_pk_fp8_f32 v232, v226, v227 op_sel:[0,0,1]
	v_cvt_pk_fp8_f32 v233, v230, v231 op_sel:[0,0,1]
	v_lshrrev_b32_e32 v234, 8, v232
	v_lshrrev_b32_e32 v235, 8, v233
	ds_write_b8 v244, v232 offset:24
	ds_write_b8 v244, v234 offset:88
	ds_write_b8_d16_hi v244, v232 offset:152
	ds_write_b8_d16_hi v244, v234 offset:216
	ds_write_b8 v244, v233 offset:264
	ds_write_b8 v244, v235 offset:328
	ds_write_b8_d16_hi v244, v233 offset:392
	ds_write_b8_d16_hi v244, v235 offset:456

.LBB0_1056:
	v_mov_b32_e32 v16, v2
	v_mov_b32_e32 v17, v2
	v_pk_mul_f32 v[34:35], v[16:17], v[22:23]
	v_pk_mul_f32 v[32:33], v[2:3], v[18:19]
	v_pk_mul_f32 v[16:17], v[16:17], v[20:21]
	v_pk_mul_f32 v[36:37], v[2:3], v[24:25]
	v_cvt_pk_bf16_f32 v32, v32, v33
	v_cvt_pk_bf16_f32 v33, v34, v35
	s_nop 0
	v_cvt_pk_bf16_f32 v34, v36, v37
	v_cvt_pk_bf16_f32 v35, v16, v17
	v_lshlrev_b32_e32 v224, 16, v32
	v_and_b32_e32 v225, 0xffff0000, v32
	v_lshlrev_b32_e32 v226, 16, v33
	v_and_b32_e32 v227, 0xffff0000, v33
	v_lshlrev_b32_e32 v228, 16, v34
	v_and_b32_e32 v229, 0xffff0000, v34
	v_lshlrev_b32_e32 v230, 16, v35
	v_and_b32_e32 v231, 0xffff0000, v35
	v_cvt_pk_fp8_f32 v232, v224, v225
	v_cvt_pk_fp8_f32 v233, v228, v229
	v_cvt_pk_fp8_f32 v232, v226, v227 op_sel:[0,0,1]
	v_cvt_pk_fp8_f32 v233, v230, v231 op_sel:[0,0,1]
	v_mov_b32_e32 v238, v232
	v_mov_b32_e32 v239, v233
	s_cbranch_execz .LBB0_994
	s_branch .LBB0_995

.LBB0_1058:
	v_mov_b32_e32 v16, v2
	v_mov_b32_e32 v17, v2
	v_pk_mul_f32 v[34:35], v[16:17], v[22:23]
	v_pk_mul_f32 v[32:33], v[2:3], v[18:19]
	v_pk_mul_f32 v[16:17], v[16:17], v[20:21]
	v_pk_mul_f32 v[36:37], v[2:3], v[24:25]
	v_cvt_pk_bf16_f32 v32, v32, v33
	v_cvt_pk_bf16_f32 v33, v34, v35
	s_nop 0
	v_cvt_pk_bf16_f32 v34, v36, v37
	v_cvt_pk_bf16_f32 v35, v16, v17
	v_lshlrev_b32_e32 v224, 16, v32
	v_and_b32_e32 v225, 0xffff0000, v32
	v_lshlrev_b32_e32 v226, 16, v33
	v_and_b32_e32 v227, 0xffff0000, v33
	v_lshlrev_b32_e32 v228, 16, v34
	v_and_b32_e32 v229, 0xffff0000, v34
	v_lshlrev_b32_e32 v230, 16, v35
	v_and_b32_e32 v231, 0xffff0000, v35
	v_cvt_pk_fp8_f32 v232, v224, v225
	v_cvt_pk_fp8_f32 v233, v228, v229
	v_cvt_pk_fp8_f32 v232, v226, v227 op_sel:[0,0,1]
	v_cvt_pk_fp8_f32 v233, v230, v231 op_sel:[0,0,1]
	v_mov_b32_e32 v240, v232
	v_mov_b32_e32 v241, v233
	s_cbranch_execz .LBB0_1004
	s_branch .LBB0_1005

.LBB0_1060:
	v_mov_b32_e32 v16, v2
	v_mov_b32_e32 v17, v2
	v_pk_mul_f32 v[34:35], v[16:17], v[22:23]
	v_pk_mul_f32 v[32:33], v[2:3], v[18:19]
	v_pk_mul_f32 v[16:17], v[16:17], v[20:21]
	v_pk_mul_f32 v[36:37], v[2:3], v[24:25]
	v_cvt_pk_bf16_f32 v32, v32, v33
	v_cvt_pk_bf16_f32 v33, v34, v35
	s_nop 0
	v_cvt_pk_bf16_f32 v34, v36, v37
	v_cvt_pk_bf16_f32 v35, v16, v17
	v_lshlrev_b32_e32 v224, 16, v32
	v_and_b32_e32 v225, 0xffff0000, v32
	v_lshlrev_b32_e32 v226, 16, v33
	v_and_b32_e32 v227, 0xffff0000, v33
	v_lshlrev_b32_e32 v228, 16, v34
	v_and_b32_e32 v229, 0xffff0000, v34
	v_lshlrev_b32_e32 v230, 16, v35
	v_and_b32_e32 v231, 0xffff0000, v35
	v_cvt_pk_fp8_f32 v232, v224, v225
	v_cvt_pk_fp8_f32 v233, v228, v229
	v_cvt_pk_fp8_f32 v232, v226, v227 op_sel:[0,0,1]
	v_cvt_pk_fp8_f32 v233, v230, v231 op_sel:[0,0,1]
	v_mov_b32_e32 v242, v232
	v_mov_b32_e32 v243, v233
	s_waitcnt lgkmcnt(0)
	ds_read_b128 v[248:251], v245
	ds_read_b128 v[224:227], v245 offset:1024
	v_readfirstlane_b32 s100, v0
	s_lshr_b32 s100, s100, 8
	s_add_i32 s100, s100, 0
	s_cmpk_lt_u32 s99, 0x80
	s_cbranch_scc0 .Lvt_c_a0
	s_and_b32 s101, s99, 63
	s_lshl_b32 s101, s101, 2
	s_add_i32 s100, s100, s101
	s_lshr_b32 s101, s99, 6
	s_branch .Lvt_j_a0
.Lvt_c_a0:
	s_addk_i32 s100, 0x100
	s_sub_i32 s101, s99, 0x80
.Lvt_j_a0:
	s_lshl_b32 s101, s101, 3
	s_add_i32 s101, s101, s98
	s_mul_i32 s101, s101, 0x104
	s_add_i32 s100, s101, s100
	s_lshl_b32 s100, s100, 13
	v_add_u32_e32 v246, s100, v252
	v_mov_b32_e32 v247, 0
	s_load_dwordx2 s[100:101], s[0:1], 0xd8
	s_waitcnt lgkmcnt(0)
	s_add_u32 s100, s100, 0x3a000000
	s_addc_u32 s101, s101, 0
	v_lshl_add_u64 v[246:247], v[246:247], 0, s[100:101]
	global_store_dwordx4 v[246:247], v[248:251], off
	global_store_dwordx4 v[246:247], v[224:227], off offset:1024
	v_lshrrev_b32_e32 v234, 8, v236
	v_lshrrev_b32_e32 v235, 8, v237
	ds_write_b8 v244, v236 offset:0
	ds_write_b8 v244, v234 offset:64
	ds_write_b8_d16_hi v244, v236 offset:128
	ds_write_b8_d16_hi v244, v234 offset:192
	ds_write_b8 v244, v237 offset:272
	ds_write_b8 v244, v235 offset:336
	ds_write_b8_d16_hi v244, v237 offset:400
	ds_write_b8_d16_hi v244, v235 offset:464
	v_lshrrev_b32_e32 v234, 8, v238
	v_lshrrev_b32_e32 v235, 8, v239
	ds_write_b8 v244, v238 offset:8
	ds_write_b8 v244, v234 offset:72
	ds_write_b8_d16_hi v244, v238 offset:136
	ds_write_b8_d16_hi v244, v234 offset:200
	ds_write_b8 v244, v239 offset:280
	ds_write_b8 v244, v235 offset:344
	ds_write_b8_d16_hi v244, v239 offset:408
	ds_write_b8_d16_hi v244, v235 offset:472
	v_lshrrev_b32_e32 v234, 8, v240
	v_lshrrev_b32_e32 v235, 8, v241
	ds_write_b8 v244, v240 offset:16
	ds_write_b8 v244, v234 offset:80
	ds_write_b8_d16_hi v244, v240 offset:144
	ds_write_b8_d16_hi v244, v234 offset:208
	ds_write_b8 v244, v241 offset:256
	ds_write_b8 v244, v235 offset:320
	ds_write_b8_d16_hi v244, v241 offset:384
	ds_write_b8_d16_hi v244, v235 offset:448
	v_lshrrev_b32_e32 v234, 8, v242
	v_lshrrev_b32_e32 v235, 8, v243
	ds_write_b8 v244, v242 offset:24
	ds_write_b8 v244, v234 offset:88
	ds_write_b8_d16_hi v244, v242 offset:152
	ds_write_b8_d16_hi v244, v234 offset:216
	ds_write_b8 v244, v243 offset:264
	ds_write_b8 v244, v235 offset:328
	ds_write_b8_d16_hi v244, v243 offset:392
	ds_write_b8_d16_hi v244, v235 offset:456
	s_mov_b32 s100, 0x208000
	s_mov_b32 s101, 0
	v_lshl_add_u64 v[246:247], v[246:247], 0, s[100:101]
	s_waitcnt lgkmcnt(0)
	ds_read_b128 v[248:251], v245
	ds_read_b128 v[224:227], v245 offset:1024
	s_waitcnt lgkmcnt(0)
	global_store_dwordx4 v[246:247], v[248:251], off
	global_store_dwordx4 v[246:247], v[224:227], off offset:1024
	s_cbranch_execz .LBB0_1014
	s_branch .LBB0_1015

.LBB0_1062:
	v_mov_b32_e32 v16, v2
	v_mov_b32_e32 v17, v2
	v_pk_mul_f32 v[34:35], v[16:17], v[22:23]
	v_pk_mul_f32 v[32:33], v[2:3], v[18:19]
	v_pk_mul_f32 v[16:17], v[16:17], v[20:21]
	v_pk_mul_f32 v[36:37], v[2:3], v[24:25]
	v_cvt_pk_bf16_f32 v32, v32, v33
	v_cvt_pk_bf16_f32 v33, v34, v35
	s_nop 0
	v_cvt_pk_bf16_f32 v34, v36, v37
	v_cvt_pk_bf16_f32 v35, v16, v17
	v_lshlrev_b32_e32 v224, 16, v32
	v_and_b32_e32 v225, 0xffff0000, v32
	v_lshlrev_b32_e32 v226, 16, v33
	v_and_b32_e32 v227, 0xffff0000, v33
	v_lshlrev_b32_e32 v228, 16, v34
	v_and_b32_e32 v229, 0xffff0000, v34
	v_lshlrev_b32_e32 v230, 16, v35
	v_and_b32_e32 v231, 0xffff0000, v35
	v_cvt_pk_fp8_f32 v232, v224, v225
	v_cvt_pk_fp8_f32 v233, v228, v229
	v_cvt_pk_fp8_f32 v232, v226, v227 op_sel:[0,0,1]
	v_cvt_pk_fp8_f32 v233, v230, v231 op_sel:[0,0,1]
	v_mov_b32_e32 v236, v232
	v_mov_b32_e32 v237, v233
	s_cbranch_execz .LBB0_1024
	s_branch .LBB0_1025

.LBB0_1068:
	v_mov_b32_e32 v12, v2
	v_mov_b32_e32 v13, v2
	v_pk_mul_f32 v[22:23], v[12:13], v[16:17]
	v_pk_mul_f32 v[20:21], v[2:3], v[10:11]
	v_pk_mul_f32 v[12:13], v[12:13], v[14:15]
	v_pk_mul_f32 v[2:3], v[2:3], v[18:19]
	v_cvt_pk_bf16_f32 v20, v20, v21
	v_cvt_pk_bf16_f32 v21, v22, v23
	s_nop 0
	v_cvt_pk_bf16_f32 v22, v2, v3
	v_cvt_pk_bf16_f32 v23, v12, v13
	v_lshlrev_b32_e32 v224, 16, v20
	v_and_b32_e32 v225, 0xffff0000, v20
	v_lshlrev_b32_e32 v226, 16, v21
	v_and_b32_e32 v227, 0xffff0000, v21
	v_lshlrev_b32_e32 v228, 16, v22
	v_and_b32_e32 v229, 0xffff0000, v22
	v_lshlrev_b32_e32 v230, 16, v23
	v_and_b32_e32 v231, 0xffff0000, v23
	v_cvt_pk_fp8_f32 v232, v224, v225
	v_cvt_pk_fp8_f32 v233, v228, v229
	v_cvt_pk_fp8_f32 v232, v226, v227 op_sel:[0,0,1]
	v_cvt_pk_fp8_f32 v233, v230, v231 op_sel:[0,0,1]
	v_mov_b32_e32 v242, v232
	v_mov_b32_e32 v243, v233
	s_waitcnt lgkmcnt(0)
	ds_read_b128 v[248:251], v245
	ds_read_b128 v[224:227], v245 offset:1024
	v_readfirstlane_b32 s100, v0
	s_lshr_b32 s100, s100, 8
	s_add_i32 s100, s100, 2
	s_cmpk_lt_u32 s99, 0x80
	s_cbranch_scc0 .Lvt_c_a1
	s_and_b32 s101, s99, 63
	s_lshl_b32 s101, s101, 2
	s_add_i32 s100, s100, s101
	s_lshr_b32 s101, s99, 6
	s_branch .Lvt_j_a1

.Lvt_j_a1:
	s_lshl_b32 s101, s101, 3
	s_add_i32 s101, s101, s98
	s_mul_i32 s101, s101, 0x104
	s_add_i32 s100, s101, s100
	s_lshl_b32 s100, s100, 13
	v_add_u32_e32 v246, s100, v252
	v_mov_b32_e32 v247, 0
	s_load_dwordx2 s[100:101], s[0:1], 0xd8
	s_waitcnt lgkmcnt(0)
	s_add_u32 s100, s100, 0x3a000000
	s_addc_u32 s101, s101, 0
	v_lshl_add_u64 v[246:247], v[246:247], 0, s[100:101]
	global_store_dwordx4 v[246:247], v[248:251], off
	global_store_dwordx4 v[246:247], v[224:227], off offset:1024
	v_lshrrev_b32_e32 v234, 8, v236
	v_lshrrev_b32_e32 v235, 8, v237
	ds_write_b8 v244, v236 offset:0
	ds_write_b8 v244, v234 offset:64
	ds_write_b8_d16_hi v244, v236 offset:128
	ds_write_b8_d16_hi v244, v234 offset:192
	ds_write_b8 v244, v237 offset:272
	ds_write_b8 v244, v235 offset:336
	ds_write_b8_d16_hi v244, v237 offset:400
	ds_write_b8_d16_hi v244, v235 offset:464
	v_lshrrev_b32_e32 v234, 8, v238
	v_lshrrev_b32_e32 v235, 8, v239
	ds_write_b8 v244, v238 offset:8
	ds_write_b8 v244, v234 offset:72
	ds_write_b8_d16_hi v244, v238 offset:136
	ds_write_b8_d16_hi v244, v234 offset:200
	ds_write_b8 v244, v239 offset:280
	ds_write_b8 v244, v235 offset:344
	ds_write_b8_d16_hi v244, v239 offset:408
	ds_write_b8_d16_hi v244, v235 offset:472
	v_lshrrev_b32_e32 v234, 8, v240
	v_lshrrev_b32_e32 v235, 8, v241
	ds_write_b8 v244, v240 offset:16
	ds_write_b8 v244, v234 offset:80
	ds_write_b8_d16_hi v244, v240 offset:144
	ds_write_b8_d16_hi v244, v234 offset:208
	ds_write_b8 v244, v241 offset:256
	ds_write_b8 v244, v235 offset:320
	ds_write_b8_d16_hi v244, v241 offset:384
	ds_write_b8_d16_hi v244, v235 offset:448
	v_lshrrev_b32_e32 v234, 8, v242
	v_lshrrev_b32_e32 v235, 8, v243
	ds_write_b8 v244, v242 offset:24
	ds_write_b8 v244, v234 offset:88
	ds_write_b8_d16_hi v244, v242 offset:152
	ds_write_b8_d16_hi v244, v234 offset:216
	ds_write_b8 v244, v243 offset:264
	ds_write_b8 v244, v235 offset:328
	ds_write_b8_d16_hi v244, v243 offset:392
	ds_write_b8_d16_hi v244, v235 offset:456
	s_mov_b32 s100, 0x208000
	s_mov_b32 s101, 0
	v_lshl_add_u64 v[246:247], v[246:247], 0, s[100:101]
	s_waitcnt lgkmcnt(0)
	ds_read_b128 v[248:251], v245
	ds_read_b128 v[224:227], v245 offset:1024
	s_waitcnt lgkmcnt(0)
	s_barrier
	global_store_dwordx4 v[246:247], v[248:251], off
	global_store_dwordx4 v[246:247], v[224:227], off offset:1024
	s_cbranch_execz .LBB0_1054

.LBB0_1127:
	s_cmp_lt_i32 s30, 11
	s_cselect_b64 s[6:7], -1, 0
	s_and_b64 s[4:5], s[6:7], s[4:5]
	s_andn2_b64 vcc, exec, s[4:5]
	s_cbranch_vccnz .LBB0_1141
	s_branch .LBB0_1141
	s_mov_b64 s[4:5], s[0:1]
	v_mbcnt_hi_u32_b32 v1, -1, v208
	s_cmpk_gt_i32 s88, 0x103f
	s_cbranch_scc1 .LBB0_1141
	s_mul_hi_i32 s3, s88, 0x7e07e07f
	s_load_dwordx2 s[10:11], s[4:5], 0xd8
	s_lshr_b32 s4, s3, 31
	s_ashr_i32 s3, s3, 7
	s_add_i32 s3, s3, s4
	s_mul_i32 s4, s3, 0x104
	s_sub_i32 s4, s88, s4
	s_ashr_i32 s9, s3, 3
	s_lshl_b32 s12, s4, 6
	s_cmpk_gt_i32 s4, 0xff
	s_cbranch_scc0 .LBB0_1131
	s_lshl_b32 s4, s9, 8
	s_add_i32 s4, s12, s4
	s_add_i32 s8, s4, 0x4000
	s_cbranch_execz .LBB0_1132
	s_branch .LBB0_1133

.LBB0_1141:
	s_cmp_gt_i32 s31, 11
	s_cselect_b64 s[4:5], -1, 0
	s_and_b64 s[6:7], s[6:7], s[4:5]
	s_andn2_b64 vcc, exec, s[6:7]
	s_branch .LBB0_1195
	s_waitcnt vmcnt(0)
	s_waitcnt lgkmcnt(0)
	s_barrier
	s_mov_b64 s[6:7], exec
	v_readlane_b32 s8, v255, 4
	v_readlane_b32 s9, v255, 5
	s_and_b64 s[8:9], s[6:7], s[8:9]
	s_mov_b64 exec, s[8:9]
	s_cbranch_execz .LBB0_1194
	s_add_i32 s3, 0, 0x23020
	v_mov_b32_e32 v1, s3
	s_waitcnt vmcnt(0) expcnt(0) lgkmcnt(0)
	ds_read_b32 v3, v1
	s_add_i32 s3, 0, 0x23024
	v_mov_b32_e32 v1, s3
	ds_read_b32 v1, v1
	s_waitcnt lgkmcnt(1)
	v_cmp_ne_u32_e32 vcc, 0, v3
	s_cbranch_vccnz .LBB0_1158
	v_readlane_b32 s8, v255, 0
	v_readlane_b32 s9, v255, 1
	s_load_dwordx2 s[12:13], s[8:9], 0x4
	s_add_u32 s8, s24, 0x4200
	s_addc_u32 s9, s25, 0
	s_add_u32 s10, s24, 0x4400
	s_addc_u32 s11, s25, 0
	s_waitcnt lgkmcnt(0)
	s_mul_i32 s3, s12, s22
	s_add_u32 s12, s24, 0x4500
	s_mul_i32 s3, s3, s13
	s_addc_u32 s13, s25, 0
	s_add_u32 s14, s24, 0x4600
	s_addc_u32 s15, s25, 0
	s_add_u32 s16, s24, 0x4700
	s_addc_u32 s17, s25, 0
	s_add_u32 s18, s24, 0x4800
	s_addc_u32 s19, s25, 0
	s_add_u32 s20, s24, 0x4900
	s_addc_u32 s21, s25, 0
	s_add_u32 s28, s24, 0x4a00
	s_addc_u32 s29, s25, 0
	s_add_u32 s38, s24, 0x4b00
	s_addc_u32 s39, s25, 0
	s_add_u32 s40, s24, 0x4c00
	s_addc_u32 s41, s25, 0
	s_add_u32 s42, s24, 0x4d00
	s_addc_u32 s43, s25, 0
	s_add_u32 s44, s24, 0x4e00
	s_addc_u32 s45, s25, 0
	s_add_u32 s46, s24, 0x4f00
	s_addc_u32 s47, s25, 0
	s_add_u32 s48, s24, 0x5000
	s_addc_u32 s49, s25, 0
	s_add_u32 s50, s24, 0x5100
	s_addc_u32 s51, s25, 0
	s_add_u32 s54, s24, 0x5200
	s_addc_u32 s55, s25, 0
	s_add_u32 s56, s24, 0x5300
	s_addc_u32 s57, s25, 0
	s_mov_b32 s23, 1
	v_mov_b32_e32 v17, 0
	s_branch .LBB0_1146
